# baseline (speedup 1.0000x reference)
.LBB0_3:
	s_load_dwordx4 s[40:43], s[0:1], 0x0
	s_load_dwordx4 s[44:47], s[0:1], 0x30
	v_cmp_lt_u32_e64 s[26:27], 63, v0
	v_cmp_gt_u32_e32 vcc, 64, v0
	s_and_saveexec_b64 s[4:5], vcc
	s_cbranch_execz .LBB0_5
	s_nop 0
	v_lshl_or_b32 v2, s2, 6, v0
	v_mov_b32_e32 v3, 0
	s_waitcnt lgkmcnt(0)
	v_lshl_add_u64 v[4:5], v[2:3], 2, s[44:45]
	global_store_dword v[4:5], v3, off
.LBB0_5:
	s_or_b64 exec, exec, s[4:5]
	s_cmp_eq_u32 s2, 0
	s_cselect_b64 s[4:5], -1, 0
	v_cmp_gt_u32_e32 vcc, 4, v0
	s_and_b64 s[6:7], s[4:5], vcc
	v_lshlrev_b32_e32 v1, 2, v0
	s_and_saveexec_b64 s[4:5], s[6:7]
	s_cbranch_execz .LBB0_7
	s_nop 0
	v_lshlrev_b32_e32 v2, 2, v0
	v_mov_b32_e32 v3, 0
	s_waitcnt lgkmcnt(0)
	global_store_dword v2, v3, s[46:47]
.LBB0_7:
	s_or_b64 exec, exec, s[4:5]
	s_nop 0
	s_movk_i32 s3, 0x188
	v_cmp_gt_u32_e32 vcc, s3, v0
	s_and_saveexec_b64 s[8:9], vcc
	s_cbranch_execz .LBB0_9
	v_lshlrev_b32_e32 v2, 2, v0
	v_mov_b32_e32 v3, 0
	ds_write_b32 v2, v3 offset:15648
	ds_write_b32 v2, v3 offset:17216
.LBB0_9:
	s_or_b64 exec, exec, s[8:9]
	s_mul_i32 s3, s2, 0xc35
	v_add_u32_e32 v2, s3, v0
	v_mov_b32_e32 v3, 0
	v_lshlrev_b64 v[4:5], 2, v[2:3]
	s_waitcnt lgkmcnt(0)
	v_lshl_add_u64 v[6:7], s[42:43], 0, v[4:5]
	v_lshl_add_u64 v[4:5], s[40:41], 0, v[4:5]
	s_barrier
	global_load_dword v10, v[4:5], off
	v_add_u32_e32 v4, 0x400, v2
	v_mov_b32_e32 v5, v3
	v_lshlrev_b64 v[4:5], 2, v[4:5]
	global_load_dword v9, v[6:7], off
	v_lshl_add_u64 v[6:7], s[42:43], 0, v[4:5]
	v_lshl_add_u64 v[4:5], s[40:41], 0, v[4:5]
	global_load_dword v12, v[4:5], off
	v_add_u32_e32 v4, 0x800, v2
	v_mov_b32_e32 v5, v3
	v_lshlrev_b64 v[4:5], 2, v[4:5]
	global_load_dword v11, v[6:7], off
	v_lshl_add_u64 v[6:7], s[42:43], 0, v[4:5]
	v_lshl_add_u64 v[4:5], s[40:41], 0, v[4:5]
	global_load_dword v13, v[6:7], off
	s_movk_i32 s8, 0xc35
	global_load_dword v4, v[4:5], off
	v_or_b32_e32 v8, 0xc00, v0
	v_cmp_gt_u32_e32 vcc, s8, v8
	s_and_saveexec_b64 s[8:9], vcc
	s_cbranch_execz .Lkp_skip
	v_add_u32_e32 v14, s3, v8
	v_mov_b32_e32 v15, 0
	v_lshlrev_b64 v[14:15], 2, v[14:15]
	v_lshl_add_u64 v[16:17], s[42:43], 0, v[14:15]
	v_lshl_add_u64 v[14:15], s[40:41], 0, v[14:15]
	global_load_dword v16, v[16:17], off
	global_load_dword v17, v[14:15], off

	.amdhsa_kernel _Z6k_partPKiS0_PjPhS1_S1_PfS3_PKfPDF16_
		.amdhsa_group_segment_fixed_size 18800
		.amdhsa_private_segment_fixed_size 0
		.amdhsa_kernarg_size 80
		.amdhsa_user_sgpr_count 2
		.amdhsa_user_sgpr_dispatch_ptr 0
		.amdhsa_user_sgpr_queue_ptr 0
		.amdhsa_user_sgpr_kernarg_segment_ptr 1
		.amdhsa_user_sgpr_dispatch_id 0
		.amdhsa_user_sgpr_kernarg_preload_length 0
		.amdhsa_user_sgpr_kernarg_preload_offset 0
		.amdhsa_user_sgpr_private_segment_size 0
		.amdhsa_uses_dynamic_stack 0
		.amdhsa_enable_private_segment 0
		.amdhsa_system_sgpr_workgroup_id_x 1
		.amdhsa_system_sgpr_workgroup_id_y 0
		.amdhsa_system_sgpr_workgroup_id_z 0
		.amdhsa_system_sgpr_workgroup_info 0
		.amdhsa_system_vgpr_workitem_id 0
		.amdhsa_next_free_vgpr 40
		.amdhsa_next_free_sgpr 48
		.amdhsa_accum_offset 40
		.amdhsa_reserve_vcc 1
		.amdhsa_float_round_mode_32 0
		.amdhsa_float_round_mode_16_64 0
		.amdhsa_float_denorm_mode_32 3
		.amdhsa_float_denorm_mode_16_64 3
		.amdhsa_dx10_clamp 1
		.amdhsa_ieee_mode 1
		.amdhsa_fp16_overflow 0
		.amdhsa_tg_split 0
		.amdhsa_exception_fp_ieee_invalid_op 0
		.amdhsa_exception_fp_denorm_src 0
		.amdhsa_exception_fp_ieee_div_zero 0
		.amdhsa_exception_fp_ieee_overflow 0
		.amdhsa_exception_fp_ieee_underflow 0
		.amdhsa_exception_fp_ieee_inexact 0
		.amdhsa_exception_int_div_zero 0
	.end_amdhsa_kernel

_Z6k_mainPKiPKjPK15HIP_vector_typeIfLj2EEPKfS8_PKDF16_S8_Pf:
	s_load_dwordx2 s[34:35], s[0:1], 0x0
	s_load_dwordx2 s[18:19], s[0:1], 0x8
	s_load_dwordx4 s[44:47], s[0:1], 0x18
	s_mul_hi_i32 s3, s2, 0xc350
	s_mul_i32 s6, s2, 0xc350
	s_lshr_b32 s4, s3, 24
	s_add_u32 s4, s6, s4
	s_addc_u32 s5, s3, 0
	s_add_i32 s3, s2, 1
	s_mul_hi_i32 s3, s3, 0xc350
	s_lshr_b64 s[24:25], s[4:5], 8
	s_add_i32 s6, s6, 0xc350
	s_lshr_b32 s4, s3, 24
	s_add_u32 s4, s6, s4
	s_addc_u32 s5, s3, 0
	s_lshr_b64 s[4:5], s[4:5], 8
	s_sub_i32 s3, s4, s24
	s_lshl_b32 s36, s24, 2
	s_add_i32 s37, s24, s3
	s_lshl_b32 s37, s37, 2
	s_lshl_b32 s30, s3, 2
	v_cmp_ge_i32_e64 s[40:41], s3, v0
	s_waitcnt lgkmcnt(0)
	s_load_dword s38, s[34:35], s36
	s_load_dword s39, s[34:35], s37
	s_and_saveexec_b64 s[42:43], s[40:41]
	s_cbranch_execz .Lrp_skip
	v_add_u32_e32 v2, s24, v0
	v_ashrrev_i32_e32 v3, 31, v2
	v_lshl_add_u64 v[2:3], v[2:3], 2, s[34:35]
	global_load_dword v1, v[2:3], off

amdhsa.kernels:
  - .agpr_count:     0
    .args:
      - .actual_access:  read_only
        .address_space:  global
        .offset:         0
        .size:           8
        .value_kind:     global_buffer
      - .actual_access:  read_only
        .address_space:  global
        .offset:         8
        .size:           8
        .value_kind:     global_buffer
      - .actual_access:  write_only
        .address_space:  global
        .offset:         16
        .size:           8
        .value_kind:     global_buffer
      - .actual_access:  write_only
        .address_space:  global
        .offset:         24
        .size:           8
        .value_kind:     global_buffer
      - .actual_access:  write_only
        .address_space:  global
        .offset:         32
        .size:           8
        .value_kind:     global_buffer
      - .actual_access:  write_only
        .address_space:  global
        .offset:         40
        .size:           8
        .value_kind:     global_buffer
      - .actual_access:  write_only
        .address_space:  global
        .offset:         48
        .size:           8
        .value_kind:     global_buffer
      - .actual_access:  write_only
        .address_space:  global
        .offset:         56
        .size:           8
        .value_kind:     global_buffer
      - .actual_access:  read_only
        .address_space:  global
        .offset:         64
        .size:           8
        .value_kind:     global_buffer
      - .actual_access:  write_only
        .address_space:  global
        .offset:         72
        .size:           8
        .value_kind:     global_buffer
    .group_segment_fixed_size: 18800
    .kernarg_segment_align: 8
    .kernarg_segment_size: 80
    .language:       OpenCL C
    .language_version:
      - 2
      - 0
    .max_flat_workgroup_size: 1024
    .name:           _Z6k_partPKiS0_PjPhS1_S1_PfS3_PKfPDF16_
    .private_segment_fixed_size: 0
    .sgpr_count:     54
    .sgpr_spill_count: 0
    .symbol:         _Z6k_partPKiS0_PjPhS1_S1_PfS3_PKfPDF16_.kd
    .uniform_work_group_size: 1
    .uses_dynamic_stack: false
    .vgpr_count:     40
    .vgpr_spill_count: 0
    .wavefront_size: 64
  - .agpr_count:     0
    .args:
      - .actual_access:  read_only
        .address_space:  global
        .offset:         0
        .size:           8
        .value_kind:     global_buffer
      - .actual_access:  read_only
        .address_space:  global
        .offset:         8
        .size:           8
        .value_kind:     global_buffer
      - .actual_access:  read_only
        .address_space:  global
        .offset:         16
        .size:           8
        .value_kind:     global_buffer
      - .actual_access:  read_only
        .address_space:  global
        .offset:         24
        .size:           8
        .value_kind:     global_buffer
      - .actual_access:  write_only
        .address_space:  global
        .offset:         32
        .size:           8
        .value_kind:     global_buffer
      - .actual_access:  write_only
        .address_space:  global
        .offset:         40
        .size:           8
        .value_kind:     global_buffer
    .group_segment_fixed_size: 3076
    .kernarg_segment_align: 8
    .kernarg_segment_size: 48
    .language:       OpenCL C
    .language_version:
      - 2
      - 0
    .max_flat_workgroup_size: 512
    .name:           _Z5k_degPKjPKhS0_S0_P15HIP_vector_typeIiLj2EEPi
    .private_segment_fixed_size: 0
    .sgpr_count:     74
    .sgpr_spill_count: 0
    .symbol:         _Z5k_degPKjPKhS0_S0_P15HIP_vector_typeIiLj2EEPi.kd
    .uniform_work_group_size: 1
    .uses_dynamic_stack: false
    .vgpr_count:     61
    .vgpr_spill_count: 0
    .wavefront_size: 64
  - .agpr_count:     0
    .args:
      - .actual_access:  read_only
        .address_space:  global
        .offset:         0
        .size:           8
        .value_kind:     global_buffer
      - .actual_access:  read_only
        .address_space:  global
        .offset:         8
        .size:           8
        .value_kind:     global_buffer
      - .actual_access:  read_only
        .address_space:  global
        .offset:         16
        .size:           8
        .value_kind:     global_buffer
      - .actual_access:  read_only
        .address_space:  global
        .offset:         24
        .size:           8
        .value_kind:     global_buffer
      - .actual_access:  write_only
        .address_space:  global
        .offset:         32
        .size:           8
        .value_kind:     global_buffer
      - .actual_access:  write_only
        .address_space:  global
        .offset:         40
        .size:           8
        .value_kind:     global_buffer
      - .actual_access:  write_only
        .address_space:  global
        .offset:         48
        .size:           8
        .value_kind:     global_buffer
    .group_segment_fixed_size: 4128
    .kernarg_segment_align: 8
    .kernarg_segment_size: 56
    .language:       OpenCL C
    .language_version:
      - 2
      - 0
    .max_flat_workgroup_size: 256
    .name:           _Z5k_csrPKjS0_PK15HIP_vector_typeIiLj2EEPKiPiPjPS1_IfLj2EE
    .private_segment_fixed_size: 0
    .sgpr_count:     74
    .sgpr_spill_count: 0
    .symbol:         _Z5k_csrPKjS0_PK15HIP_vector_typeIiLj2EEPKiPiPjPS1_IfLj2EE.kd
    .uniform_work_group_size: 1
    .uses_dynamic_stack: false
    .vgpr_count:     126
    .vgpr_spill_count: 0
    .wavefront_size: 64
  - .agpr_count:     0
    .args:
      - .actual_access:  read_only
        .address_space:  global
        .offset:         0
        .size:           8
        .value_kind:     global_buffer
      - .actual_access:  read_only
        .address_space:  global
        .offset:         8
        .size:           8
        .value_kind:     global_buffer
      - .actual_access:  read_only
        .address_space:  global
        .offset:         16
        .size:           8
        .value_kind:     global_buffer
      - .actual_access:  read_only
        .address_space:  global
        .offset:         24
        .size:           8
        .value_kind:     global_buffer
      - .actual_access:  read_only
        .address_space:  global
        .offset:         32
        .size:           8
        .value_kind:     global_buffer
      - .actual_access:  read_only
        .address_space:  global
        .offset:         40
        .size:           8
        .value_kind:     global_buffer
      - .actual_access:  read_only
        .address_space:  global
        .offset:         48
        .size:           8
        .value_kind:     global_buffer
      - .address_space:  global
        .offset:         56
        .size:           8
        .value_kind:     global_buffer
    .group_segment_fixed_size: 151664
    .kernarg_segment_align: 8
    .kernarg_segment_size: 64
    .language:       OpenCL C
    .language_version:
      - 2
      - 0
    .max_flat_workgroup_size: 1024
    .name:           _Z6k_mainPKiPKjPK15HIP_vector_typeIfLj2EEPKfS8_PKDF16_S8_Pf
    .private_segment_fixed_size: 0
    .sgpr_count:     84
    .sgpr_spill_count: 0
    .symbol:         _Z6k_mainPKiPKjPK15HIP_vector_typeIfLj2EEPKfS8_PKDF16_S8_Pf.kd
    .uniform_work_group_size: 1
    .uses_dynamic_stack: false
    .vgpr_count:     128
    .vgpr_spill_count: 0
    .wavefront_size: 64
  - .agpr_count:     0
    .args:
      - .actual_access:  read_only
        .address_space:  global
        .offset:         0
        .size:           8
        .value_kind:     global_buffer
      - .actual_access:  read_only
        .address_space:  global
        .offset:         8
        .size:           8
        .value_kind:     global_buffer
      - .actual_access:  read_only
        .address_space:  global
        .offset:         16
        .size:           8
        .value_kind:     global_buffer
      - .actual_access:  read_only
        .address_space:  global
        .offset:         24
        .size:           8
        .value_kind:     global_buffer
      - .actual_access:  read_only
        .address_space:  global
        .offset:         32
        .size:           8
        .value_kind:     global_buffer
      - .actual_access:  read_only
        .address_space:  global
        .offset:         40
        .size:           8
        .value_kind:     global_buffer
      - .actual_access:  read_only
        .address_space:  global
        .offset:         48
        .size:           8
        .value_kind:     global_buffer
      - .actual_access:  read_only
        .address_space:  global
        .offset:         56
        .size:           8
        .value_kind:     global_buffer
      - .actual_access:  read_only
        .address_space:  global
        .offset:         64
        .size:           8
        .value_kind:     global_buffer
      - .actual_access:  read_only
        .address_space:  global
        .offset:         72
        .size:           8
        .value_kind:     global_buffer
      - .address_space:  global
        .offset:         80
        .size:           8
        .value_kind:     global_buffer
    .group_segment_fixed_size: 2688
    .kernarg_segment_align: 8
    .kernarg_segment_size: 88
    .language:       OpenCL C
    .language_version:
      - 2
      - 0
    .max_flat_workgroup_size: 256
    .name:           _Z7k_finalPKfS0_S0_S0_S0_S0_S0_S0_S0_S0_Pf
    .private_segment_fixed_size: 0
    .sgpr_count:     54
    .sgpr_spill_count: 0
    .symbol:         _Z7k_finalPKfS0_S0_S0_S0_S0_S0_S0_S0_S0_Pf.kd
    .uniform_work_group_size: 1
    .uses_dynamic_stack: false
    .vgpr_count:     256
    .vgpr_spill_count: 0
    .wavefront_size: 64
